# speedup vs baseline: 1.0150x; 1.0071x over previous
_Z9k2_colsumPKDv8_DF16_S1_Pf:
	s_load_dwordx4 s[4:7], s[0:1], 0x0
	s_load_dwordx2 s[8:9], s[0:1], 0x10
	v_mov_b32_e32 v170, v0
	v_and_b32_e32 v172, 63, v0
	v_lshrrev_b32_e32 v173, 6, v0
	v_lshlrev_b32_e32 v171, 4, v172
	v_add_u32_e32 v174, 0x1000, v171
	s_lshr_b32 s10, s2, 6
	s_and_b32 s11, s2, 63
	s_lshl_b32 s11, s11, 1
	s_lshl_b32 s12, s10, 7
	s_add_u32 s13, s12, s11
	s_lshl_b32 s13, s13, 12
	v_readfirstlane_b32 s14, v173
	s_nop 3
	s_lshl_b32 s15, s14, 4
	s_add_u32 s15, s15, s12
	s_lshl_b32 s15, s15, 12
	s_waitcnt lgkmcnt(0)
	s_add_u32 s6, s6, s13
	s_addc_u32 s7, s7, 0
	s_add_u32 s4, s4, s15
	s_addc_u32 s5, s5, 0
	global_load_dwordx4 v[0:3], v171, s[6:7] offset:0
	global_load_dwordx4 v[4:7], v171, s[6:7] offset:1024
	global_load_dwordx4 v[8:11], v171, s[6:7] offset:2048
	global_load_dwordx4 v[12:15], v171, s[6:7] offset:3072
	global_load_dwordx4 v[16:19], v174, s[6:7] offset:0
	global_load_dwordx4 v[20:23], v174, s[6:7] offset:1024
	global_load_dwordx4 v[24:27], v174, s[6:7] offset:2048
	global_load_dwordx4 v[28:31], v174, s[6:7] offset:3072
	global_load_dwordx4 v[32:35], v171, s[4:5] offset:0
	global_load_dwordx4 v[36:39], v171, s[4:5] offset:1024
	global_load_dwordx4 v[40:43], v171, s[4:5] offset:2048
	global_load_dwordx4 v[44:47], v171, s[4:5] offset:3072
	s_add_u32 s4, s4, 0x1000
	s_addc_u32 s5, s5, 0
	global_load_dwordx4 v[48:51], v171, s[4:5] offset:0
	global_load_dwordx4 v[52:55], v171, s[4:5] offset:1024
	global_load_dwordx4 v[56:59], v171, s[4:5] offset:2048
	global_load_dwordx4 v[60:63], v171, s[4:5] offset:3072
	s_add_u32 s4, s4, 0x1000
	s_addc_u32 s5, s5, 0
	global_load_dwordx4 v[64:67], v171, s[4:5] offset:0
	global_load_dwordx4 v[68:71], v171, s[4:5] offset:1024
	global_load_dwordx4 v[72:75], v171, s[4:5] offset:2048
	global_load_dwordx4 v[76:79], v171, s[4:5] offset:3072
	s_add_u32 s4, s4, 0x1000
	s_addc_u32 s5, s5, 0
	global_load_dwordx4 v[80:83], v171, s[4:5] offset:0
	global_load_dwordx4 v[84:87], v171, s[4:5] offset:1024
	global_load_dwordx4 v[88:91], v171, s[4:5] offset:2048
	global_load_dwordx4 v[92:95], v171, s[4:5] offset:3072
	s_add_u32 s4, s4, 0x1000
	s_addc_u32 s5, s5, 0
	v_mov_b32_e32 v160, 0
	v_mov_b32_e32 v161, 0
	v_mov_b32_e32 v162, 0
	v_mov_b32_e32 v163, 0
	v_mov_b32_e32 v164, 0
	v_mov_b32_e32 v165, 0
	v_mov_b32_e32 v166, 0
	v_mov_b32_e32 v167, 0
	s_cmp_lt_u32 s14, 4
	s_cbranch_scc1 .Lk2_older
	s_setprio 1
	s_sleep 2
